# P11 EpiDown row-gate loads preloaded (were serialised by register reuse); P4 bisection padding nops removed; S5 state GEMM units moved to the lighter CUs 0-127
# speedup vs baseline: 1.0087x; 1.0087x over previous
; #define PG8_WAIT_V(n) asm volatile("s_waitcnt vmcnt(" #n ")" ::: "memory")
; template <class Epi, class Sched, bool ALIGN_EPI = false, bool SP2 = false, bool F8 = false, bool GATHER = false>
; __device__ __forceinline__ void gemm_phase(PG8_LAS unsigned char* lds, const Gemm g, const Sched& S, const Epi& E) {
;     const int tid = threadIdx.x, wid = __builtin_amdgcn_readfirstlane(tid >> 6), lane = tid & 63, wr = wid >> 2, wc = wid & 3, fr = lane & 15, fq = lane >> 4;
;     const int K = g.K, nt = K / BK;
;     unsigned voffA[2], voffB[2];
; #pragma unroll
;     for (int i = 0; i < 2; ++i) { int R, C; stage_rc(tid * 16 + i * 8192, R, C); const int Rb = Epi::PERM ? ((R & ~31) + perm32(R & 31)) : R;
;         voffA[i] = (unsigned)(R * g.lda + C) * 2u; voffB[i] = (unsigned)(Rb * g.ldb + C) * 2u; }
;     unsigned gC0[2] = {0u, 0u}, gC1[2] = {0u, 0u}, gN0[2] = {0u, 0u}, gN1[2] = {0u, 0u}; int gR[2] = {0, 0}; unsigned gCb[2] = {0u, 0u};
;     if constexpr (GATHER) {
; #pragma unroll
;         for (int i = 0; i < 2; ++i) { int R, C; stage_rc(tid * 16 + i * 8192, R, C); gR[i] = R; gCb[i] = (unsigned)C * 2u; } }
;     ...
;     const size_t kstep = (size_t)(BK * 2);
;     const size_t hstepA = (size_t)HALF * g.lda * 2, hstepB = (size_t)HALF * g.ldb * 2;
;     const size_t tstepA = 2 * hstepA, tstepB = 2 * hstepB;
;     const unsigned ldsw = (unsigned)wid * 1024u;
;     const int aoff = lds_byte(wr * 64 + fr, fq * 8), boff = lds_byte(wc * 32 + fr, fq * 8);
;     ...
;     Unit cur, nxt; int ui = 0;
;     if (!S.next(0, cur)) return;
;     f32x4 acc[2][2][4][2];
; #pragma unroll
;     for (int a = 0; a < 2; ++a)
; #pragma unroll
;         for (int b = 0; b < 2; ++b)
; #pragma unroll
;             for (int m = 0; m < 4; ++m)
; #pragma unroll
;                 for (int n = 0; n < 2; ++n) acc[a][b][m][n] = (f32x4){0.f, 0.f, 0.f, 0.f};
;     FragT<F8> At[4], B0[2], B1[2];
;     const char* cA = (const char*)g.A + (GATHER ? (size_t)0 : (size_t)cur.pm * tstepA); const char* cB = (const char*)g.Bt + (size_t)cur.pn * tstepB;
;     if constexpr (GATHER) { PG8_GROWS(gC0, gC1, 0); }
;     S.a_ready(cur);
;     if constexpr (SP2) {
;         PG8_STAGE(PG8_SB(0, 0), cB, voffB); PG8_STAGE(PG8_SB(0, 1), cB + hstepB, voffB); PG8_STAGE_A(PG8_SA(0, 0), cA, 0, false); PG8_STAGE_A(PG8_SA(0, 1), cA, 1, false);
;         if (wr == 1) PG8_BAR;
;         PG8_WAIT_V(2); PG8_BAR;
.LBB0_592:
	s_mov_b32 s24, s84
	v_lshlrev_b32_e32 v78, 2, v0
	s_cmpk_gt_i32 s24, 0x7f
	v_readfirstlane_b32 s4, v0
	s_barrier
	s_cbranch_scc1 .LBB0_608
	s_lshr_b32 s2, s4, 6
	s_lshr_b32 s3, s4, 8
	s_lshl_b32 s10, s2, 10
	s_add_u32 s25, s82, 0x31400000
	s_addc_u32 s26, s83, 0
	s_add_u32 s27, s82, 0x4100000
	v_or_b32_e32 v2, 0x2000, v179
	s_addc_u32 s28, s83, 0
	s_ashr_i32 s0, s24, 1
	v_lshrrev_b32_e32 v2, 7, v2
	v_bfe_u32 v3, v0, 2, 4
	s_movk_i32 s1, 0x70
	v_and_or_b32 v2, v2, s1, v3
	s_ashr_i32 s1, s0, 31
	s_lshl_b64 s[0:1], s[0:1], 18
	s_add_u32 s18, s27, s0
	s_addc_u32 s19, s28, s1
	s_add_u32 s0, s18, 0x20000
	v_and_b32_e32 v4, 32, v0
	s_mul_i32 s8, s24, 0x50000
	s_addc_u32 s1, s19, 0
	s_waitcnt vmcnt(3)
	v_bitop3_b32 v10, v179, v4, 48 bitop3:0x6c
	v_and_b32_e32 v11, 64, v0
	s_mul_hi_i32 s5, s24, 0x50000
	s_add_u32 s16, s25, s8
	v_or_b32_e32 v4, v10, v11
	s_addc_u32 s17, s26, s5
	v_lshl_or_b32 v66, v2, 10, v4
	v_mul_u32_u24_e32 v12, 0x500, v2
	v_lshrrev_b32_e32 v2, 3, v0
	s_add_u32 s8, s16, 0x28000
	v_and_or_b32 v2, v2, 48, v3
	s_addc_u32 s9, s17, 0
	s_add_i32 s29, s10, 0
	v_lshl_or_b32 v70, v2, 10, v4
	s_add_i32 m0, s29, 0x10000
	s_add_i32 s30, s29, 0x14000
	global_load_lds_dwordx4 v70, s[18:19]
	s_add_i32 m0, s29, 0x12000
	s_add_i32 s31, s29, 0x16000
	global_load_lds_dwordx4 v66, s[18:19]
	s_mov_b32 m0, s30
	v_mul_u32_u24_e32 v13, 0x500, v2
	global_load_lds_dwordx4 v70, s[0:1]
	s_mov_b32 m0, s31
	v_or_b32_e32 v72, v4, v13
	global_load_lds_dwordx4 v66, s[0:1]
	s_mov_b32 m0, s29
	s_add_i32 s33, s29, 0x2000
	v_or_b32_e32 v68, v12, v4
	global_load_lds_dwordx4 v72, s[16:17]
	s_mov_b32 m0, s33
	s_add_i32 s34, s29, 0x4000
	global_load_lds_dwordx4 v68, s[16:17]
	s_mov_b32 m0, s34
	s_add_i32 s35, s29, 0x6000
	global_load_lds_dwordx4 v72, s[8:9]
	s_mov_b32 m0, s35
	v_mov_b32_e32 v71, 0
	global_load_lds_dwordx4 v68, s[8:9]
	v_mov_b32_e32 v67, v71
	v_mov_b32_e32 v73, v71
	v_mov_b32_e32 v69, v71
	s_cmp_eq_u32 s3, 1
	v_lshl_add_u64 v[2:3], s[18:19], 0, v[70:71]
	v_lshl_add_u64 v[4:5], s[18:19], 0, v[66:67]
	v_lshl_add_u64 v[6:7], s[16:17], 0, v[72:73]
	v_lshl_add_u64 v[8:9], s[16:17], 0, v[68:69]
	s_cselect_b64 s[0:1], -1, 0
	s_cmp_lg_u32 s3, 1
	s_mov_b32 s36, 0
	s_cbranch_scc1 .LBB0_595
	s_barrier

; template <int NVM> __device__ __forceinline__ int cnt_ge(const unsigned (&key)[32], unsigned cand) {
;     unsigned c0 = 0, c1 = 0, c2 = 0, c3 = 0;
; #pragma unroll
;     for (int i = 0; i < NVM; i += 4) {
;         asm("v_cmp_ge_u32 vcc, %1, %2\n\tv_addc_co_u32 %0, vcc, 0, %0, vcc" : "+v"(c0) : "v"(key[i]), "v"(cand) : "vcc");
;         asm("v_cmp_ge_u32 vcc, %1, %2\n\tv_addc_co_u32 %0, vcc, 0, %0, vcc" : "+v"(c1) : "v"(key[i + 1]), "v"(cand) : "vcc");
;         asm("v_cmp_ge_u32 vcc, %1, %2\n\tv_addc_co_u32 %0, vcc, 0, %0, vcc" : "+v"(c2) : "v"(key[i + 2]), "v"(cand) : "vcc");
;         asm("v_cmp_ge_u32 vcc, %1, %2\n\tv_addc_co_u32 %0, vcc, 0, %0, vcc" : "+v"(c3) : "v"(key[i + 3]), "v"(cand) : "vcc"); }
;     const unsigned c = (c0 + c1) + (c2 + c3);
;     int tot = 0;
; #pragma unroll
;     for (int b = 0; b < 6; ++b) tot += __builtin_popcountll(__ballot((c >> b) & 1u)) << b;
;     return tot;
; }
; template <int NVM> __device__ __forceinline__ unsigned sel_thr(const unsigned (&key)[32]) {
;     unsigned Tt = 0u;
;     ...
;         if (cnt >= TOPK) { Tt = cand; if (cnt == TOPK) break; } }
;     return Tt;
; }
.LBB0_705:
	v_lshlrev_b32_e64 v85, v84, 1
	v_mov_b32_e32 v86, 0
	v_or_b32_e32 v85, v85, v66
	v_cmp_ge_u32 vcc, v5, v85
	v_addc_co_u32 v86, vcc, 0, v86, vcc
	v_mov_b32_e32 v87, 0
	v_cmp_ge_u32 vcc, v36, v85
	v_addc_co_u32 v87, vcc, 0, v87, vcc
	v_mov_b32_e32 v88, 0
	v_mov_b32_e32 v89, 0
	v_cmp_ge_u32 vcc, v39, v85
	v_addc_co_u32 v86, vcc, 0, v86, vcc
	v_cmp_ge_u32 vcc, v37, v85
	v_addc_co_u32 v88, vcc, 0, v88, vcc
	v_cmp_ge_u32 vcc, v38, v85
	v_addc_co_u32 v89, vcc, 0, v89, vcc
	v_cmp_ge_u32 vcc, v67, v85
	v_addc_co_u32 v87, vcc, 0, v87, vcc
	v_cmp_ge_u32 vcc, v43, v85
	v_addc_co_u32 v86, vcc, 0, v86, vcc
	v_cmp_ge_u32 vcc, v68, v85
	v_addc_co_u32 v88, vcc, 0, v88, vcc
	v_cmp_ge_u32 vcc, v69, v85
	v_addc_co_u32 v89, vcc, 0, v89, vcc
	v_cmp_ge_u32 vcc, v70, v85
	v_addc_co_u32 v87, vcc, 0, v87, vcc
	v_cmp_ge_u32 vcc, v73, v85
	v_addc_co_u32 v86, vcc, 0, v86, vcc
	v_cmp_ge_u32 vcc, v71, v85
	v_addc_co_u32 v88, vcc, 0, v88, vcc
	v_cmp_ge_u32 vcc, v72, v85
	v_addc_co_u32 v89, vcc, 0, v89, vcc
	v_cmp_ge_u32 vcc, v74, v85
	v_addc_co_u32 v87, vcc, 0, v87, vcc
	v_cmp_ge_u32 vcc, v52, v85
	v_addc_co_u32 v86, vcc, 0, v86, vcc
	v_cmp_ge_u32 vcc, v75, v85
	v_addc_co_u32 v88, vcc, 0, v88, vcc
	v_cmp_ge_u32 vcc, v76, v85
	v_addc_co_u32 v89, vcc, 0, v89, vcc
	v_cmp_ge_u32 vcc, v77, v85
	v_addc_co_u32 v87, vcc, 0, v87, vcc
	v_cmp_ge_u32 vcc, v80, v85
	v_addc_co_u32 v86, vcc, 0, v86, vcc
	v_cmp_ge_u32 vcc, v78, v85
	v_addc_co_u32 v88, vcc, 0, v88, vcc
	v_cmp_ge_u32 vcc, v79, v85
	v_addc_co_u32 v89, vcc, 0, v89, vcc
	v_cmp_ge_u32 vcc, v81, v85
	v_addc_co_u32 v87, vcc, 0, v87, vcc
	v_cmp_ge_u32 vcc, v62, v85
	v_addc_co_u32 v86, vcc, 0, v86, vcc
	v_cmp_ge_u32 vcc, v82, v85
	v_addc_co_u32 v88, vcc, 0, v88, vcc
	v_cmp_ge_u32 vcc, v83, v85
	v_addc_co_u32 v89, vcc, 0, v89, vcc
	v_cmp_ge_u32 vcc, v58, v85
	v_addc_co_u32 v87, vcc, 0, v87, vcc
	v_cmp_ge_u32 vcc, v61, v85
	v_addc_co_u32 v86, vcc, 0, v86, vcc
	v_cmp_ge_u32 vcc, v59, v85
	v_addc_co_u32 v88, vcc, 0, v88, vcc
	v_cmp_ge_u32 vcc, v60, v85
	v_addc_co_u32 v89, vcc, 0, v89, vcc
	v_cmp_ge_u32 vcc, v63, v85
	v_addc_co_u32 v87, vcc, 0, v87, vcc
	v_add_u32_e32 v86, v87, v86
	v_cmp_ge_u32 vcc, v64, v85
	v_addc_co_u32 v88, vcc, 0, v88, vcc
	v_cmp_ge_u32 vcc, v65, v85
	v_addc_co_u32 v89, vcc, 0, v89, vcc
	v_add3_u32 v86, v86, v88, v89
	v_and_b32_e32 v87, 1, v86
	v_cmp_ne_u32_e32 vcc, 0, v87
	v_bfe_u32 v87, v86, 1, 1
	s_bcnt1_i32_b64 s6, vcc
	v_cmp_ne_u32_e32 vcc, 0, v87
	s_bcnt1_i32_b64 s7, vcc
	v_bfe_u32 v87, v86, 2, 1
	s_lshl_b32 s7, s7, 1
	v_cmp_ne_u32_e32 vcc, 0, v87
	s_add_i32 s6, s7, s6
	s_bcnt1_i32_b64 s7, vcc
	v_bfe_u32 v87, v86, 3, 1
	s_lshl_b32 s7, s7, 2
	v_cmp_ne_u32_e32 vcc, 0, v87
	s_add_i32 s6, s6, s7
	s_bcnt1_i32_b64 s7, vcc
	v_bfe_u32 v87, v86, 4, 1
	s_lshl_b32 s7, s7, 3
	v_cmp_ne_u32_e32 vcc, 0, v87
	s_add_i32 s6, s6, s7
	s_bcnt1_i32_b64 s7, vcc
	v_bfe_u32 v86, v86, 5, 1
	s_lshl_b32 s7, s7, 4
	v_cmp_ne_u32_e32 vcc, 0, v86
	s_add_i32 s6, s6, s7
	s_bcnt1_i32_b64 s7, vcc
	s_lshl_b32 s7, s7, 5
	s_add_i32 s8, s6, s7
	s_cmpk_eq_i32 s8, 0x100
	s_cselect_b64 s[6:7], -1, 0
	s_cmpk_lt_u32 s8, 0x100
	s_cselect_b64 vcc, -1, 0
	v_cndmask_b32_e32 v66, v85, v66, vcc
	v_subrev_co_u32_e32 v84, vcc, 1, v84
	s_or_b64 s[6:7], s[6:7], vcc
	s_andn2_b64 vcc, exec, s[6:7]
	s_cbranch_vccnz .LBB0_705
	s_branch .LBB0_712

; template <int NVM> __device__ __forceinline__ int cnt_ge(const unsigned (&key)[32], unsigned cand) {
;     unsigned c0 = 0, c1 = 0, c2 = 0, c3 = 0;
; #pragma unroll
;     for (int i = 0; i < NVM; i += 4) {
;         asm("v_cmp_ge_u32 vcc, %1, %2\n\tv_addc_co_u32 %0, vcc, 0, %0, vcc" : "+v"(c0) : "v"(key[i]), "v"(cand) : "vcc");
;         asm("v_cmp_ge_u32 vcc, %1, %2\n\tv_addc_co_u32 %0, vcc, 0, %0, vcc" : "+v"(c1) : "v"(key[i + 1]), "v"(cand) : "vcc");
;         asm("v_cmp_ge_u32 vcc, %1, %2\n\tv_addc_co_u32 %0, vcc, 0, %0, vcc" : "+v"(c2) : "v"(key[i + 2]), "v"(cand) : "vcc");
;         asm("v_cmp_ge_u32 vcc, %1, %2\n\tv_addc_co_u32 %0, vcc, 0, %0, vcc" : "+v"(c3) : "v"(key[i + 3]), "v"(cand) : "vcc"); }
;     const unsigned c = (c0 + c1) + (c2 + c3);
;     int tot = 0;
; #pragma unroll
;     for (int b = 0; b < 6; ++b) tot += __builtin_popcountll(__ballot((c >> b) & 1u)) << b;
;     return tot;
; }
; template <int NVM> __device__ __forceinline__ unsigned sel_thr(const unsigned (&key)[32]) {
;     unsigned Tt = 0u;
;     ...
;         if (cnt >= TOPK) { Tt = cand; if (cnt == TOPK) break; } }
;     return Tt;
; }
.LBB0_711:
	v_lshlrev_b32_e64 v78, v77, 1
	v_mov_b32_e32 v79, 0
	v_or_b32_e32 v78, v78, v66
	v_cmp_ge_u32 vcc, v5, v78
	v_addc_co_u32 v79, vcc, 0, v79, vcc
	v_mov_b32_e32 v80, 0
	v_cmp_ge_u32 vcc, v36, v78
	v_addc_co_u32 v80, vcc, 0, v80, vcc
	v_mov_b32_e32 v81, 0
	v_mov_b32_e32 v82, 0
	v_cmp_ge_u32 vcc, v39, v78
	v_addc_co_u32 v79, vcc, 0, v79, vcc
	v_cmp_ge_u32 vcc, v37, v78
	v_addc_co_u32 v81, vcc, 0, v81, vcc
	v_cmp_ge_u32 vcc, v38, v78
	v_addc_co_u32 v82, vcc, 0, v82, vcc
	v_cmp_ge_u32 vcc, v67, v78
	v_addc_co_u32 v80, vcc, 0, v80, vcc
	v_cmp_ge_u32 vcc, v43, v78
	v_addc_co_u32 v79, vcc, 0, v79, vcc
	v_cmp_ge_u32 vcc, v68, v78
	v_addc_co_u32 v81, vcc, 0, v81, vcc
	v_cmp_ge_u32 vcc, v69, v78
	v_addc_co_u32 v82, vcc, 0, v82, vcc
	v_cmp_ge_u32 vcc, v70, v78
	v_addc_co_u32 v80, vcc, 0, v80, vcc
	v_cmp_ge_u32 vcc, v73, v78
	v_addc_co_u32 v79, vcc, 0, v79, vcc
	v_cmp_ge_u32 vcc, v71, v78
	v_addc_co_u32 v81, vcc, 0, v81, vcc
	v_cmp_ge_u32 vcc, v72, v78
	v_addc_co_u32 v82, vcc, 0, v82, vcc
	v_cmp_ge_u32 vcc, v74, v78
	v_addc_co_u32 v80, vcc, 0, v80, vcc
	v_cmp_ge_u32 vcc, v52, v78
	v_addc_co_u32 v79, vcc, 0, v79, vcc
	v_cmp_ge_u32 vcc, v75, v78
	v_addc_co_u32 v81, vcc, 0, v81, vcc
	v_cmp_ge_u32 vcc, v76, v78
	v_addc_co_u32 v82, vcc, 0, v82, vcc
	v_cmp_ge_u32 vcc, v50, v78
	v_addc_co_u32 v80, vcc, 0, v80, vcc
	v_cmp_ge_u32 vcc, v54, v78
	v_addc_co_u32 v79, vcc, 0, v79, vcc
	v_cmp_ge_u32 vcc, v51, v78
	v_addc_co_u32 v81, vcc, 0, v81, vcc
	v_cmp_ge_u32 vcc, v53, v78
	v_addc_co_u32 v82, vcc, 0, v82, vcc
	v_cmp_ge_u32 vcc, v55, v78
	v_addc_co_u32 v80, vcc, 0, v80, vcc
	v_add_u32_e32 v79, v80, v79
	v_cmp_ge_u32 vcc, v56, v78
	v_addc_co_u32 v81, vcc, 0, v81, vcc
	v_cmp_ge_u32 vcc, v57, v78
	v_addc_co_u32 v82, vcc, 0, v82, vcc
	v_add3_u32 v79, v79, v81, v82
	v_and_b32_e32 v80, 1, v79
	v_cmp_ne_u32_e32 vcc, 0, v80
	v_bfe_u32 v80, v79, 1, 1
	s_bcnt1_i32_b64 s6, vcc
	v_cmp_ne_u32_e32 vcc, 0, v80
	s_bcnt1_i32_b64 s7, vcc
	v_bfe_u32 v80, v79, 2, 1
	s_lshl_b32 s7, s7, 1
	v_cmp_ne_u32_e32 vcc, 0, v80
	s_add_i32 s6, s7, s6
	s_bcnt1_i32_b64 s7, vcc
	v_bfe_u32 v80, v79, 3, 1
	s_lshl_b32 s7, s7, 2
	v_cmp_ne_u32_e32 vcc, 0, v80
	s_add_i32 s6, s6, s7
	s_bcnt1_i32_b64 s7, vcc
	v_bfe_u32 v80, v79, 4, 1
	s_lshl_b32 s7, s7, 3
	v_cmp_ne_u32_e32 vcc, 0, v80
	s_add_i32 s6, s6, s7
	s_bcnt1_i32_b64 s7, vcc
	v_bfe_u32 v79, v79, 5, 1
	s_lshl_b32 s7, s7, 4
	v_cmp_ne_u32_e32 vcc, 0, v79
	s_add_i32 s6, s6, s7
	s_bcnt1_i32_b64 s7, vcc
	s_lshl_b32 s7, s7, 5
	s_add_i32 s8, s6, s7
	s_cmpk_eq_i32 s8, 0x100
	s_cselect_b64 s[6:7], -1, 0
	s_cmpk_lt_u32 s8, 0x100
	s_cselect_b64 vcc, -1, 0
	v_cndmask_b32_e32 v66, v78, v66, vcc
	v_subrev_co_u32_e32 v77, vcc, 1, v77
	s_or_b64 s[6:7], s[6:7], vcc
	s_and_b64 vcc, exec, s[6:7]
	s_cbranch_vccz .LBB0_711

; template <int NVM> __device__ __forceinline__ int cnt_ge(const unsigned (&key)[32], unsigned cand) {
;     unsigned c0 = 0, c1 = 0, c2 = 0, c3 = 0;
; #pragma unroll
;     for (int i = 0; i < NVM; i += 4) {
;         asm("v_cmp_ge_u32 vcc, %1, %2\n\tv_addc_co_u32 %0, vcc, 0, %0, vcc" : "+v"(c0) : "v"(key[i]), "v"(cand) : "vcc");
;         asm("v_cmp_ge_u32 vcc, %1, %2\n\tv_addc_co_u32 %0, vcc, 0, %0, vcc" : "+v"(c1) : "v"(key[i + 1]), "v"(cand) : "vcc");
;         asm("v_cmp_ge_u32 vcc, %1, %2\n\tv_addc_co_u32 %0, vcc, 0, %0, vcc" : "+v"(c2) : "v"(key[i + 2]), "v"(cand) : "vcc");
;         asm("v_cmp_ge_u32 vcc, %1, %2\n\tv_addc_co_u32 %0, vcc, 0, %0, vcc" : "+v"(c3) : "v"(key[i + 3]), "v"(cand) : "vcc"); }
;     const unsigned c = (c0 + c1) + (c2 + c3);
;     int tot = 0;
; #pragma unroll
;     for (int b = 0; b < 6; ++b) tot += __builtin_popcountll(__ballot((c >> b) & 1u)) << b;
;     return tot;
; }
; template <int NVM> __device__ __forceinline__ unsigned sel_thr(const unsigned (&key)[32]) {
;     unsigned Tt = 0u;
;     ...
;         if (cnt >= TOPK) { Tt = cand; if (cnt == TOPK) break; } }
;     return Tt;
; }
.LBB0_714:
	v_lshlrev_b32_e64 v71, v70, 1
	v_mov_b32_e32 v72, 0
	v_or_b32_e32 v71, v71, v66
	v_cmp_ge_u32 vcc, v5, v71
	v_addc_co_u32 v72, vcc, 0, v72, vcc
	v_mov_b32_e32 v73, 0
	v_cmp_ge_u32 vcc, v36, v71
	v_addc_co_u32 v73, vcc, 0, v73, vcc
	v_mov_b32_e32 v74, 0
	v_mov_b32_e32 v75, 0
	v_cmp_ge_u32 vcc, v39, v71
	v_addc_co_u32 v72, vcc, 0, v72, vcc
	v_cmp_ge_u32 vcc, v37, v71
	v_addc_co_u32 v74, vcc, 0, v74, vcc
	v_cmp_ge_u32 vcc, v38, v71
	v_addc_co_u32 v75, vcc, 0, v75, vcc
	v_cmp_ge_u32 vcc, v67, v71
	v_addc_co_u32 v73, vcc, 0, v73, vcc
	v_cmp_ge_u32 vcc, v43, v71
	v_addc_co_u32 v72, vcc, 0, v72, vcc
	v_cmp_ge_u32 vcc, v68, v71
	v_addc_co_u32 v74, vcc, 0, v74, vcc
	v_cmp_ge_u32 vcc, v69, v71
	v_addc_co_u32 v75, vcc, 0, v75, vcc
	v_cmp_ge_u32 vcc, v42, v71
	v_addc_co_u32 v73, vcc, 0, v73, vcc
	v_cmp_ge_u32 vcc, v46, v71
	v_addc_co_u32 v72, vcc, 0, v72, vcc
	v_cmp_ge_u32 vcc, v44, v71
	v_addc_co_u32 v74, vcc, 0, v74, vcc
	v_cmp_ge_u32 vcc, v45, v71
	v_addc_co_u32 v75, vcc, 0, v75, vcc
	v_cmp_ge_u32 vcc, v47, v71
	v_addc_co_u32 v73, vcc, 0, v73, vcc
	v_add_u32_e32 v72, v73, v72
	v_cmp_ge_u32 vcc, v48, v71
	v_addc_co_u32 v74, vcc, 0, v74, vcc
	v_cmp_ge_u32 vcc, v49, v71
	v_addc_co_u32 v75, vcc, 0, v75, vcc
	v_add3_u32 v72, v72, v74, v75
	v_and_b32_e32 v73, 1, v72
	v_cmp_ne_u32_e32 vcc, 0, v73
	v_bfe_u32 v73, v72, 1, 1
	s_bcnt1_i32_b64 s6, vcc
	v_cmp_ne_u32_e32 vcc, 0, v73
	s_bcnt1_i32_b64 s7, vcc
	v_bfe_u32 v73, v72, 2, 1
	s_lshl_b32 s7, s7, 1
	v_cmp_ne_u32_e32 vcc, 0, v73
	s_add_i32 s6, s7, s6
	s_bcnt1_i32_b64 s7, vcc
	v_bfe_u32 v73, v72, 3, 1
	s_lshl_b32 s7, s7, 2
	v_cmp_ne_u32_e32 vcc, 0, v73
	s_add_i32 s6, s6, s7
	s_bcnt1_i32_b64 s7, vcc
	v_bfe_u32 v73, v72, 4, 1
	s_lshl_b32 s7, s7, 3
	v_cmp_ne_u32_e32 vcc, 0, v73
	s_add_i32 s6, s6, s7
	s_bcnt1_i32_b64 s7, vcc
	v_bfe_u32 v72, v72, 5, 1
	s_lshl_b32 s7, s7, 4
	v_cmp_ne_u32_e32 vcc, 0, v72
	s_add_i32 s6, s6, s7
	s_bcnt1_i32_b64 s7, vcc
	s_lshl_b32 s7, s7, 5
	s_add_i32 s8, s6, s7
	s_cmpk_eq_i32 s8, 0x100
	s_cselect_b64 s[6:7], -1, 0
	s_cmpk_lt_u32 s8, 0x100
	s_cselect_b64 vcc, -1, 0
	v_cndmask_b32_e32 v66, v71, v66, vcc
	v_subrev_co_u32_e32 v70, vcc, 1, v70
	s_or_b64 s[6:7], s[6:7], vcc
	s_and_b64 vcc, exec, s[6:7]
	s_cbranch_vccz .LBB0_714

; template <int NVM> __device__ __forceinline__ int cnt_ge(const unsigned (&key)[32], unsigned cand) {
;     unsigned c0 = 0, c1 = 0, c2 = 0, c3 = 0;
; #pragma unroll
;     for (int i = 0; i < NVM; i += 4) {
;         asm("v_cmp_ge_u32 vcc, %1, %2\n\tv_addc_co_u32 %0, vcc, 0, %0, vcc" : "+v"(c0) : "v"(key[i]), "v"(cand) : "vcc");
;         asm("v_cmp_ge_u32 vcc, %1, %2\n\tv_addc_co_u32 %0, vcc, 0, %0, vcc" : "+v"(c1) : "v"(key[i + 1]), "v"(cand) : "vcc");
;         asm("v_cmp_ge_u32 vcc, %1, %2\n\tv_addc_co_u32 %0, vcc, 0, %0, vcc" : "+v"(c2) : "v"(key[i + 2]), "v"(cand) : "vcc");
;         asm("v_cmp_ge_u32 vcc, %1, %2\n\tv_addc_co_u32 %0, vcc, 0, %0, vcc" : "+v"(c3) : "v"(key[i + 3]), "v"(cand) : "vcc"); }
;     const unsigned c = (c0 + c1) + (c2 + c3);
;     int tot = 0;
; #pragma unroll
;     for (int b = 0; b < 6; ++b) tot += __builtin_popcountll(__ballot((c >> b) & 1u)) << b;
;     return tot;
; }
; template <int NVM> __device__ __forceinline__ unsigned sel_thr(const unsigned (&key)[32]) {
;     unsigned Tt = 0u;
;     ...
;         if (cnt >= TOPK) { Tt = cand; if (cnt == TOPK) break; } }
;     return Tt;
; }
.LBB0_717:
	v_lshlrev_b32_e64 v68, v67, 1
	v_mov_b32_e32 v69, 0
	v_or_b32_e32 v68, v68, v66
	v_cmp_ge_u32 vcc, v5, v68
	v_addc_co_u32 v69, vcc, 0, v69, vcc
	v_mov_b32_e32 v70, 0
	v_cmp_ge_u32 vcc, v36, v68
	v_addc_co_u32 v70, vcc, 0, v70, vcc
	v_mov_b32_e32 v71, 0
	v_mov_b32_e32 v72, 0
	v_cmp_ge_u32 vcc, v39, v68
	v_addc_co_u32 v69, vcc, 0, v69, vcc
	v_cmp_ge_u32 vcc, v37, v68
	v_addc_co_u32 v71, vcc, 0, v71, vcc
	v_cmp_ge_u32 vcc, v38, v68
	v_addc_co_u32 v72, vcc, 0, v72, vcc
	v_cmp_ge_u32 vcc, v35, v68
	v_addc_co_u32 v70, vcc, 0, v70, vcc
	v_add_u32_e32 v69, v70, v69
	v_cmp_ge_u32 vcc, v40, v68
	v_addc_co_u32 v71, vcc, 0, v71, vcc
	v_cmp_ge_u32 vcc, v41, v68
	v_addc_co_u32 v72, vcc, 0, v72, vcc
	v_add3_u32 v69, v69, v71, v72
	v_and_b32_e32 v70, 1, v69
	v_cmp_ne_u32_e32 vcc, 0, v70
	v_bfe_u32 v70, v69, 1, 1
	s_bcnt1_i32_b64 s6, vcc
	v_cmp_ne_u32_e32 vcc, 0, v70
	s_bcnt1_i32_b64 s7, vcc
	v_bfe_u32 v70, v69, 2, 1
	s_lshl_b32 s7, s7, 1
	v_cmp_ne_u32_e32 vcc, 0, v70
	s_add_i32 s6, s7, s6
	s_bcnt1_i32_b64 s7, vcc
	v_bfe_u32 v70, v69, 3, 1
	s_lshl_b32 s7, s7, 2
	v_cmp_ne_u32_e32 vcc, 0, v70
	s_add_i32 s6, s6, s7
	s_bcnt1_i32_b64 s7, vcc
	v_bfe_u32 v70, v69, 4, 1
	s_lshl_b32 s7, s7, 3
	v_cmp_ne_u32_e32 vcc, 0, v70
	s_add_i32 s6, s6, s7
	s_bcnt1_i32_b64 s7, vcc
	v_bfe_u32 v69, v69, 5, 1
	s_lshl_b32 s7, s7, 4
	v_cmp_ne_u32_e32 vcc, 0, v69
	s_add_i32 s6, s6, s7
	s_bcnt1_i32_b64 s7, vcc
	s_lshl_b32 s7, s7, 5
	s_add_i32 s8, s6, s7
	s_cmpk_eq_i32 s8, 0x100
	s_cselect_b64 s[6:7], -1, 0
	s_cmpk_lt_u32 s8, 0x100
	s_cselect_b64 vcc, -1, 0
	v_cndmask_b32_e32 v66, v68, v66, vcc
	v_subrev_co_u32_e32 v67, vcc, 1, v67
	s_or_b64 s[6:7], s[6:7], vcc
	s_and_b64 vcc, exec, s[6:7]
	s_cbranch_vccz .LBB0_717

; template <class Epi, class Sched, bool ALIGN_EPI = false, bool SP2 = false, bool F8 = false, bool GATHER = false>
; __device__ __forceinline__ void gemm_phase(PG8_LAS unsigned char* lds, const Gemm g, const Sched& S, const Epi& E) {
;     ...
;         if constexpr (F8) asm volatile("s_nop 15\n\ts_nop 15" ::: "memory");
;     __device__ __forceinline__ void operator()(const f32x4 (&acc)[2][2][4][2], const Unit& u, int wr, int wc, int fr, int fq) const {
;         const int e = (u.pn >> 3) & 31, ct = u.pn & 7, row0 = u.pm * 256 + wr * 64 + fr, col0 = ct * 256 + wc * 32 + 8 * fq, ne = mt[32 + e], i0 = row0 - mt[e];
;         f32x4 bv[2][2]; float grv[2][4];
; #pragma unroll
;         for (int bj = 0; bj < 2; ++bj) { const float* bp = bd + (size_t)e * 2048 + col0 + bj * 128; bv[bj][0] = *(const f32x4*)bp; bv[bj][1] = *(const f32x4*)(bp + 4); }
; #pragma unroll
;         for (int ai = 0; ai < 2; ++ai)
; #pragma unroll
;             for (int m = 0; m < 4; ++m) { const int idx = i0 + ai * 128 + m * 16; const bool ok = idx >= 0 && idx < ne && idx < T; const float gl = GLIST[(size_t)e * T + (ok ? idx : 0)]; grv[ai][m] = ok ? gl * F8_YSCALE : 0.f; }
; #pragma unroll
;         for (int ai = 0; ai < 2; ++ai)
; #pragma unroll
;             for (int m = 0; m < 4; ++m) { const size_t row = (size_t)(row0 + ai * 128 + m * 16); const float gr = grv[ai][m];
; #pragma unroll
;                 for (int bj = 0; bj < 2; ++bj) { const int col = col0 + bj * 128;
;                     const f32x4 y0 = (acc[ai][bj][m][0] * F8_DESCALE + bv[bj][0]) * gr, y1 = (acc[ai][bj][m][1] * F8_DESCALE + bv[bj][1]) * gr;
;                     v2u w8; w8.x = pk4_fp8(y0[0], y0[1], y0[2], y0[3]); w8.y = pk4_fp8(y1[0], y1[1], y1[2], y1[3]); *(v2u*)(YE + row * 2048 + col) = w8; } }
.LBB0_1528:
	s_lshl_b32 s0, s0, 8
	s_add_i32 s35, s0, s62
	s_lshl_b32 s0, s42, 8
	s_and_b32 s0, s0, 0x700
	v_mov_b32_e32 v20, v1
	v_mov_b32_e32 v2, v179
	s_bfe_u32 s31, s42, 0x50003
	s_or_b32 s0, s0, s63
	s_nop 15
	s_nop 15
	v_readlane_b32 s80, v250, 3
	v_lshl_add_u32 v22, v2, 3, s0
	s_lshl_b32 s0, s31, 2
	s_add_i32 s0, s0, 0
	s_add_i32 s0, s0, 0x20400
	v_mov_b32_e32 v2, s0
	ds_read2_b32 v[18:19], v2 offset1:32
	v_readlane_b32 s86, v250, 9
	v_readlane_b32 s87, v250, 10
	s_lshl_b32 s0, s31, 13
	s_mov_b64 s[42:43], s[86:87]
	s_add_u32 s0, s42, s0
	s_addc_u32 s1, s43, 0
	v_ashrrev_i32_e32 v23, 31, v22
	v_add_u32_e32 v176, s35, v20
	v_lshl_add_u64 v[6:7], v[22:23], 2, s[0:1]
	s_waitcnt lgkmcnt(0)
	v_sub_u32_e32 v18, v176, v18
	s_lshl_b32 s0, s31, 16
	s_add_u32 s42, s64, s0
	v_cmp_lt_i32_e32 vcc, v18, v19
	v_cmp_gt_u32_e64 s[0:1], s61, v18
	s_addc_u32 s43, s65, 0
	s_and_b64 vcc, s[0:1], vcc
	v_ashrrev_i32_e32 v20, 31, v18
	v_cndmask_b32_e32 v21, 0, v20, vcc
	v_cndmask_b32_e32 v20, 0, v18, vcc
	v_lshl_add_u64 v[20:21], v[20:21], 2, s[42:43]
	v_mov_b32_e32 v199, 0
	v_add_u32_e32 v198, 0x10, v18
	v_cmp_lt_i32_e64 s[98:99], v198, v19
	v_cmp_gt_u32_e64 s[100:101], s61, v198
	s_and_b64 s[98:99], s[98:99], s[100:101]
	s_nop 0
	v_cndmask_b32_e64 v198, 0, v198, s[98:99]
	v_lshl_add_u64 v[200:201], v[198:199], 2, s[42:43]
	global_load_dword v191, v[200:201], off
	v_add_u32_e32 v198, 0x20, v18
	v_cmp_lt_i32_e64 s[98:99], v198, v19
	v_cmp_gt_u32_e64 s[100:101], s61, v198
	s_and_b64 s[98:99], s[98:99], s[100:101]
	s_nop 0
	v_cndmask_b32_e64 v198, 0, v198, s[98:99]
	v_lshl_add_u64 v[202:203], v[198:199], 2, s[42:43]
	global_load_dword v192, v[202:203], off
	v_add_u32_e32 v198, 0x30, v18
	v_cmp_lt_i32_e64 s[98:99], v198, v19
	v_cmp_gt_u32_e64 s[100:101], s61, v198
	s_and_b64 s[98:99], s[98:99], s[100:101]
	s_nop 0
	v_cndmask_b32_e64 v198, 0, v198, s[98:99]
	v_lshl_add_u64 v[200:201], v[198:199], 2, s[42:43]
	global_load_dword v193, v[200:201], off
	v_add_u32_e32 v198, 0x80, v18
	v_cmp_lt_i32_e64 s[98:99], v198, v19
	v_cmp_gt_u32_e64 s[100:101], s61, v198
	s_and_b64 s[98:99], s[98:99], s[100:101]
	s_nop 0
	v_cndmask_b32_e64 v198, 0, v198, s[98:99]
	v_lshl_add_u64 v[202:203], v[198:199], 2, s[42:43]
	global_load_dword v194, v[202:203], off
	v_add_u32_e32 v198, 0x90, v18
	v_cmp_lt_i32_e64 s[98:99], v198, v19
	v_cmp_gt_u32_e64 s[100:101], s61, v198
	s_and_b64 s[98:99], s[98:99], s[100:101]
	s_nop 0
	v_cndmask_b32_e64 v198, 0, v198, s[98:99]
	v_lshl_add_u64 v[200:201], v[198:199], 2, s[42:43]
	global_load_dword v195, v[200:201], off
	v_add_u32_e32 v198, 0xa0, v18
	v_cmp_lt_i32_e64 s[98:99], v198, v19
	v_cmp_gt_u32_e64 s[100:101], s61, v198
	s_and_b64 s[98:99], s[98:99], s[100:101]
	s_nop 0
	v_cndmask_b32_e64 v198, 0, v198, s[98:99]
	v_lshl_add_u64 v[202:203], v[198:199], 2, s[42:43]
	global_load_dword v196, v[202:203], off
	v_add_u32_e32 v198, 0xb0, v18
	v_cmp_lt_i32_e64 s[98:99], v198, v19
	v_cmp_gt_u32_e64 s[100:101], s61, v198
	s_and_b64 s[98:99], s[98:99], s[100:101]
	s_nop 0
	v_cndmask_b32_e64 v198, 0, v198, s[98:99]
	v_lshl_add_u64 v[200:201], v[198:199], 2, s[42:43]
	global_load_dword v197, v[200:201], off
	global_load_dwordx4 v[10:13], v[6:7], off offset:16
	global_load_dwordx4 v[14:17], v[6:7], off
	global_load_dwordx4 v[2:5], v[6:7], off offset:528
	s_nop 0
	global_load_dwordx4 v[6:9], v[6:7], off offset:512
	v_ashrrev_i32_e32 v177, 31, v176
	global_load_dword v20, v[20:21], off
	v_lshlrev_b64 v[176:177], 11, v[176:177]
	v_readlane_b32 s81, v250, 4
	v_readlane_b32 s82, v250, 5
	v_readlane_b32 s83, v250, 6
	v_readlane_b32 s84, v250, 7
	v_readlane_b32 s80, v250, 51
	v_readlane_b32 s84, v250, 50
	v_readlane_b32 s81, v250, 52
	v_readlane_b32 s82, v250, 53
	v_readlane_b32 s83, v250, 54
	v_readlane_b32 s85, v250, 8
	s_waitcnt vmcnt(0)
	v_pk_fma_f32 v[154:155], v[154:155], s[16:17], v[10:11] op_sel_hi:[1,0,1]
	v_pk_fma_f32 v[158:159], v[158:159], s[16:17], v[14:15] op_sel_hi:[1,0,1]
	v_pk_fma_f32 v[146:147], v[146:147], s[16:17], v[2:3] op_sel_hi:[1,0,1]
	v_pk_fma_f32 v[150:151], v[150:151], s[16:17], v[6:7] op_sel_hi:[1,0,1]
	v_pk_fma_f32 v[160:161], v[160:161], s[16:17], v[16:17] op_sel_hi:[1,0,1]
	v_mul_f32_e32 v20, 0x41000000, v20
	v_cndmask_b32_e32 v174, 0, v20, vcc
	v_add_u32_e32 v20, 16, v18
	v_cmp_lt_i32_e32 vcc, v20, v19
	v_cmp_gt_u32_e64 s[0:1], s61, v20
	s_and_b64 vcc, s[0:1], vcc
	v_ashrrev_i32_e32 v21, 31, v20
	v_cndmask_b32_e32 v21, 0, v21, vcc
	v_cndmask_b32_e32 v20, 0, v20, vcc
	v_lshl_add_u64 v[20:21], v[20:21], 2, s[42:43]
	v_mov_b32_e32 v20, v191
	v_pk_mul_f32 v[158:159], v[158:159], v[174:175] op_sel_hi:[1,0]
	v_pk_mul_f32 v[154:155], v[154:155], v[174:175] op_sel_hi:[1,0]
	v_pk_mul_f32 v[150:151], v[150:151], v[174:175] op_sel_hi:[1,0]
	v_pk_mul_f32 v[146:147], v[146:147], v[174:175] op_sel_hi:[1,0]
	v_pk_fma_f32 v[142:143], v[142:143], s[16:17], v[14:15] op_sel_hi:[1,0,1]
	v_pk_mul_f32 v[160:161], v[160:161], v[174:175] op_sel_hi:[1,0]
	v_pk_fma_f32 v[156:157], v[156:157], s[16:17], v[12:13] op_sel_hi:[1,0,1]
	v_pk_fma_f32 v[138:139], v[138:139], s[16:17], v[10:11] op_sel_hi:[1,0,1]
	v_pk_mul_f32 v[156:157], v[156:157], v[174:175] op_sel_hi:[1,0]
	v_med3_f32 v25, v160, s73, v188
	v_med3_f32 v27, v161, s73, v188
	v_pk_fma_f32 v[152:153], v[152:153], s[16:17], v[8:9] op_sel_hi:[1,0,1]
	v_pk_fma_f32 v[134:135], v[134:135], s[16:17], v[6:7] op_sel_hi:[1,0,1]
	v_pk_mul_f32 v[152:153], v[152:153], v[174:175] op_sel_hi:[1,0]
	v_pk_fma_f32 v[148:149], v[148:149], s[16:17], v[4:5] op_sel_hi:[1,0,1]
	v_pk_fma_f32 v[144:145], v[144:145], s[16:17], v[16:17] op_sel_hi:[1,0,1]
	v_pk_fma_f32 v[140:141], v[140:141], s[16:17], v[12:13] op_sel_hi:[1,0,1]
	v_pk_fma_f32 v[136:137], v[136:137], s[16:17], v[8:9] op_sel_hi:[1,0,1]
	v_pk_fma_f32 v[132:133], v[132:133], s[16:17], v[4:5] op_sel_hi:[1,0,1]
	v_pk_fma_f32 v[130:131], v[130:131], s[16:17], v[2:3] op_sel_hi:[1,0,1]
	v_pk_mul_f32 v[148:149], v[148:149], v[174:175] op_sel_hi:[1,0]
	v_pk_fma_f32 v[126:127], v[126:127], s[16:17], v[14:15] op_sel_hi:[1,0,1]
	v_pk_fma_f32 v[122:123], v[122:123], s[16:17], v[10:11] op_sel_hi:[1,0,1]
	v_pk_fma_f32 v[124:125], v[124:125], s[16:17], v[12:13] op_sel_hi:[1,0,1]
	v_pk_fma_f32 v[118:119], v[118:119], s[16:17], v[6:7] op_sel_hi:[1,0,1]
	v_pk_fma_f32 v[116:117], v[116:117], s[16:17], v[4:5] op_sel_hi:[1,0,1]
	v_pk_fma_f32 v[114:115], v[114:115], s[16:17], v[2:3] op_sel_hi:[1,0,1]
	v_pk_fma_f32 v[106:107], v[106:107], s[16:17], v[10:11] op_sel_hi:[1,0,1]
	v_pk_fma_f32 v[108:109], v[108:109], s[16:17], v[12:13] op_sel_hi:[1,0,1]
	v_pk_fma_f32 v[102:103], v[102:103], s[16:17], v[6:7] op_sel_hi:[1,0,1]
	v_pk_fma_f32 v[100:101], v[100:101], s[16:17], v[4:5] op_sel_hi:[1,0,1]
	v_pk_fma_f32 v[98:99], v[98:99], s[16:17], v[2:3] op_sel_hi:[1,0,1]
	v_pk_fma_f32 v[90:91], v[90:91], s[16:17], v[10:11] op_sel_hi:[1,0,1]
	v_pk_fma_f32 v[84:85], v[84:85], s[16:17], v[4:5] op_sel_hi:[1,0,1]
	v_pk_fma_f32 v[82:83], v[82:83], s[16:17], v[2:3] op_sel_hi:[1,0,1]
	v_pk_fma_f32 v[66:67], v[66:67], s[16:17], v[2:3] op_sel_hi:[1,0,1]
	s_waitcnt vmcnt(0)
;     __device__ __forceinline__ void operator()(const f32x4 (&acc)[2][2][4][2], const Unit& u, int wr, int wc, int fr, int fq) const {
;     ...
;             for (int m = 0; m < 4; ++m) { const int idx = i0 + ai * 128 + m * 16; const bool ok = idx >= 0 && idx < ne && idx < T; const float gl = GLIST[(size_t)e * T + (ok ? idx : 0)]; grv[ai][m] = ok ? gl * F8_YSCALE : 0.f; }
; #pragma unroll
;         for (int ai = 0; ai < 2; ++ai)
; #pragma unroll
;             for (int m = 0; m < 4; ++m) { const size_t row = (size_t)(row0 + ai * 128 + m * 16); const float gr = grv[ai][m];
; #pragma unroll
;                 for (int bj = 0; bj < 2; ++bj) { const int col = col0 + bj * 128;
;                     const f32x4 y0 = (acc[ai][bj][m][0] * F8_DESCALE + bv[bj][0]) * gr, y1 = (acc[ai][bj][m][1] * F8_DESCALE + bv[bj][1]) * gr;
;                     v2u w8; w8.x = pk4_fp8(y0[0], y0[1], y0[2], y0[3]); w8.y = pk4_fp8(y1[0], y1[1], y1[2], y1[3]); *(v2u*)(YE + row * 2048 + col) = w8; } }
	v_mul_f32_e32 v20, 0x41000000, v20
	v_cndmask_b32_e32 v32, 0, v20, vcc
	v_add_u32_e32 v20, 32, v18
	v_cmp_lt_i32_e32 vcc, v20, v19
	v_cmp_gt_u32_e64 s[0:1], s61, v20
	s_and_b64 vcc, s[0:1], vcc
	v_ashrrev_i32_e32 v21, 31, v20
	v_cndmask_b32_e32 v21, 0, v21, vcc
	v_cndmask_b32_e32 v20, 0, v20, vcc
	v_lshl_add_u64 v[20:21], v[20:21], 2, s[42:43]
	v_mov_b32_e32 v20, v192
	v_pk_mul_f32 v[142:143], v[142:143], v[32:33] op_sel_hi:[1,0]
	v_pk_mul_f32 v[138:139], v[138:139], v[32:33] op_sel_hi:[1,0]
	v_pk_mul_f32 v[134:135], v[134:135], v[32:33] op_sel_hi:[1,0]
	v_pk_mul_f32 v[144:145], v[144:145], v[32:33] op_sel_hi:[1,0]
	v_pk_mul_f32 v[140:141], v[140:141], v[32:33] op_sel_hi:[1,0]
	v_pk_mul_f32 v[136:137], v[136:137], v[32:33] op_sel_hi:[1,0]
	v_pk_mul_f32 v[132:133], v[132:133], v[32:33] op_sel_hi:[1,0]
	v_pk_mul_f32 v[32:33], v[130:131], v[32:33] op_sel_hi:[1,0]
	v_mov_b32_e32 v130, 0
	v_mov_b32_e32 v131, 0
	s_waitcnt vmcnt(0)
	v_mul_f32_e32 v20, 0x41000000, v20
	v_cndmask_b32_e32 v30, 0, v20, vcc
	v_add_u32_e32 v20, 48, v18
	v_cmp_lt_i32_e32 vcc, v20, v19
	v_cmp_gt_u32_e64 s[0:1], s61, v20
	s_and_b64 vcc, s[0:1], vcc
	v_ashrrev_i32_e32 v21, 31, v20
	v_cndmask_b32_e32 v21, 0, v21, vcc
	v_cndmask_b32_e32 v20, 0, v20, vcc
	v_lshl_add_u64 v[20:21], v[20:21], 2, s[42:43]
	v_mov_b32_e32 v20, v193
	v_pk_mul_f32 v[126:127], v[126:127], v[30:31] op_sel_hi:[1,0]
	v_pk_mul_f32 v[122:123], v[122:123], v[30:31] op_sel_hi:[1,0]
	v_pk_mul_f32 v[124:125], v[124:125], v[30:31] op_sel_hi:[1,0]
	v_pk_mul_f32 v[118:119], v[118:119], v[30:31] op_sel_hi:[1,0]
	v_pk_mul_f32 v[116:117], v[116:117], v[30:31] op_sel_hi:[1,0]
	s_waitcnt vmcnt(0)
	v_mul_f32_e32 v20, 0x41000000, v20
	v_cndmask_b32_e32 v28, 0, v20, vcc
	v_add_u32_e32 v20, 0x80, v18
	v_cmp_lt_i32_e32 vcc, v20, v19
	v_cmp_gt_u32_e64 s[0:1], s61, v20
	s_and_b64 vcc, s[0:1], vcc
	v_ashrrev_i32_e32 v21, 31, v20
	v_cndmask_b32_e32 v21, 0, v21, vcc
	v_cndmask_b32_e32 v20, 0, v20, vcc
	v_lshl_add_u64 v[20:21], v[20:21], 2, s[42:43]
	v_mov_b32_e32 v20, v194
	v_pk_mul_f32 v[106:107], v[106:107], v[28:29] op_sel_hi:[1,0]
	v_pk_mul_f32 v[108:109], v[108:109], v[28:29] op_sel_hi:[1,0]
	v_pk_mul_f32 v[102:103], v[102:103], v[28:29] op_sel_hi:[1,0]
	v_pk_mul_f32 v[100:101], v[100:101], v[28:29] op_sel_hi:[1,0]
	s_waitcnt vmcnt(0)
	v_mul_f32_e32 v20, 0x41000000, v20
	v_cndmask_b32_e32 v26, 0, v20, vcc
	v_add_u32_e32 v20, 0x90, v18
	v_cmp_lt_i32_e32 vcc, v20, v19
	v_cmp_gt_u32_e64 s[0:1], s61, v20
	s_and_b64 vcc, s[0:1], vcc
	v_ashrrev_i32_e32 v21, 31, v20
	v_cndmask_b32_e32 v21, 0, v21, vcc
	v_cndmask_b32_e32 v20, 0, v20, vcc
	v_lshl_add_u64 v[20:21], v[20:21], 2, s[42:43]
	v_mov_b32_e32 v20, v195
	s_waitcnt vmcnt(0)
	v_mul_f32_e32 v20, 0x41000000, v20
	v_cndmask_b32_e32 v24, 0, v20, vcc
	v_add_u32_e32 v20, 0xa0, v18
	v_cmp_lt_i32_e32 vcc, v20, v19
	v_cmp_gt_u32_e64 s[0:1], s61, v20
	s_and_b64 vcc, s[0:1], vcc
	v_ashrrev_i32_e32 v21, 31, v20
	v_cndmask_b32_e32 v21, 0, v21, vcc
	v_cndmask_b32_e32 v20, 0, v20, vcc
	v_lshl_add_u64 v[20:21], v[20:21], 2, s[42:43]
	v_mov_b32_e32 v20, v196
	v_add_u32_e32 v18, 0xb0, v18
	v_cmp_gt_u32_e64 s[0:1], s61, v18
	v_med3_f32 v21, v159, s73, v188
	v_mov_b32_e32 v159, 0
	s_waitcnt vmcnt(0)
	v_mul_f32_e32 v20, 0x41000000, v20
	v_cndmask_b32_e32 v20, 0, v20, vcc
	v_cmp_lt_i32_e32 vcc, v18, v19
	s_and_b64 vcc, s[0:1], vcc
	v_ashrrev_i32_e32 v19, 31, v18
	v_cndmask_b32_e32 v19, 0, v19, vcc
	v_cndmask_b32_e32 v18, 0, v18, vcc
	v_lshl_add_u64 v[18:19], v[18:19], 2, s[42:43]
	v_mov_b32_e32 v18, v197
	v_med3_f32 v19, v158, s73, v188
	v_mov_b32_e32 v158, 0
	v_cvt_pk_fp8_f32 v158, v19, v21
	v_med3_f32 v19, v154, s73, v188
	v_med3_f32 v21, v155, s73, v188
	v_cvt_pk_fp8_f32 v159, v19, v21
	v_med3_f32 v19, v150, s73, v188
	v_med3_f32 v21, v151, s73, v188
	v_mov_b32_e32 v150, 0
	v_cvt_pk_fp8_f32 v150, v19, v21
	v_med3_f32 v19, v146, s73, v188
	v_med3_f32 v21, v147, s73, v188
	v_mov_b32_e32 v151, 0
	v_cvt_pk_fp8_f32 v151, v19, v21
	v_med3_f32 v19, v142, s73, v188
	v_med3_f32 v21, v143, s73, v188
	v_mov_b32_e32 v142, 0
	v_cvt_pk_fp8_f32 v158, v25, v27 op_sel:[0,0,1]
	v_med3_f32 v25, v156, s73, v188
	v_med3_f32 v27, v157, s73, v188
	v_cvt_pk_fp8_f32 v142, v19, v21
	v_med3_f32 v19, v138, s73, v188
	v_med3_f32 v21, v139, s73, v188
	v_mov_b32_e32 v143, 0
	v_cvt_pk_fp8_f32 v159, v25, v27 op_sel:[0,0,1]
	v_med3_f32 v25, v152, s73, v188
	v_med3_f32 v27, v153, s73, v188
	v_cvt_pk_fp8_f32 v143, v19, v21
	v_med3_f32 v19, v134, s73, v188
	v_med3_f32 v21, v135, s73, v188
	v_cvt_pk_fp8_f32 v150, v25, v27 op_sel:[0,0,1]
	v_med3_f32 v25, v148, s73, v188
	v_med3_f32 v27, v149, s73, v188
	v_cvt_pk_fp8_f32 v130, v19, v21
	v_med3_f32 v19, v32, s73, v188
	v_med3_f32 v21, v33, s73, v188
	v_cvt_pk_fp8_f32 v151, v25, v27 op_sel:[0,0,1]
	v_med3_f32 v25, v144, s73, v188
	v_med3_f32 v27, v145, s73, v188
	v_cvt_pk_fp8_f32 v131, v19, v21
	v_cvt_pk_fp8_f32 v142, v25, v27 op_sel:[0,0,1]
	v_med3_f32 v25, v140, s73, v188
	v_med3_f32 v27, v141, s73, v188
	v_cvt_pk_fp8_f32 v143, v25, v27 op_sel:[0,0,1]
	v_med3_f32 v25, v136, s73, v188
	v_med3_f32 v27, v137, s73, v188
	v_pk_fma_f32 v[32:33], v[128:129], s[16:17], v[16:17] op_sel_hi:[1,0,1]
	v_cvt_pk_fp8_f32 v130, v25, v27 op_sel:[0,0,1]
	v_med3_f32 v25, v132, s73, v188
	v_med3_f32 v27, v133, s73, v188
	v_pk_mul_f32 v[32:33], v[32:33], v[30:31] op_sel_hi:[1,0]
	v_cvt_pk_fp8_f32 v131, v25, v27 op_sel:[0,0,1]
	v_med3_f32 v19, v126, s73, v188
	v_med3_f32 v21, v127, s73, v188
	v_med3_f32 v25, v32, s73, v188
	v_mov_b32_e32 v32, 0
	v_med3_f32 v27, v33, s73, v188
	v_cvt_pk_fp8_f32 v32, v19, v21
	v_med3_f32 v19, v122, s73, v188
	v_med3_f32 v21, v123, s73, v188
	v_mov_b32_e32 v33, 0
	v_cvt_pk_fp8_f32 v33, v19, v21
	v_lshl_add_u64 v[154:155], s[10:11], 0, v[176:177]
	v_lshl_add_u64 v[22:23], v[154:155], 0, v[22:23]
	v_cvt_pk_fp8_f32 v32, v25, v27 op_sel:[0,0,1]
	v_med3_f32 v25, v124, s73, v188
	v_med3_f32 v27, v125, s73, v188
	v_cvt_pk_fp8_f32 v33, v25, v27 op_sel:[0,0,1]
	v_med3_f32 v19, v118, s73, v188
	v_med3_f32 v21, v119, s73, v188
	v_lshl_add_u64 v[122:123], v[22:23], 0, s[20:21]
	v_lshl_add_u64 v[138:139], v[22:23], 0, s[18:19]
	s_mov_b64 s[0:1], -1
	global_store_dwordx2 v[22:23], v[158:159], off
	global_store_dwordx2 v[22:23], v[150:151], off offset:128
	global_store_dwordx2 v[138:139], v[130:131], off offset:128
	s_waitcnt vmcnt(3)
;     __device__ __forceinline__ void operator()(const f32x4 (&acc)[2][2][4][2], const Unit& u, int wr, int wc, int fr, int fq) const {
;     ...
;             for (int m = 0; m < 4; ++m) { const size_t row = (size_t)(row0 + ai * 128 + m * 16); const float gr = grv[ai][m];
; #pragma unroll
;                 for (int bj = 0; bj < 2; ++bj) { const int col = col0 + bj * 128;
;                     const f32x4 y0 = (acc[ai][bj][m][0] * F8_DESCALE + bv[bj][0]) * gr, y1 = (acc[ai][bj][m][1] * F8_DESCALE + bv[bj][1]) * gr;
;                     v2u w8; w8.x = pk4_fp8(y0[0], y0[1], y0[2], y0[3]); w8.y = pk4_fp8(y1[0], y1[1], y1[2], y1[3]); *(v2u*)(YE + row * 2048 + col) = w8; } }
	v_mul_f32_e32 v18, 0x41000000, v18
	v_cndmask_b32_e32 v18, 0, v18, vcc
	v_add_co_u32_e32 v140, vcc, s70, v22
	s_nop 1
	v_addc_co_u32_e32 v141, vcc, 0, v23, vcc
	v_add_co_u32_e32 v124, vcc, s60, v22
	global_store_dwordx2 v[140:141], v[142:143], off
	s_nop 0
	v_addc_co_u32_e32 v125, vcc, 0, v23, vcc
	global_store_dwordx2 v[124:125], v[32:33], off
	v_pk_fma_f32 v[32:33], v[120:121], s[16:17], v[8:9] op_sel_hi:[1,0,1]
	s_nop 0
	v_pk_mul_f32 v[32:33], v[32:33], v[30:31] op_sel_hi:[1,0]
	v_pk_mul_f32 v[30:31], v[114:115], v[30:31] op_sel_hi:[1,0]
	v_med3_f32 v25, v32, s73, v188
	v_mov_b32_e32 v32, 0
	v_med3_f32 v27, v33, s73, v188
	v_cvt_pk_fp8_f32 v32, v19, v21
	v_med3_f32 v19, v30, s73, v188
	v_med3_f32 v21, v31, s73, v188
	v_mov_b32_e32 v33, 0
	v_cvt_pk_fp8_f32 v33, v19, v21
	v_cvt_pk_fp8_f32 v32, v25, v27 op_sel:[0,0,1]
	v_med3_f32 v25, v116, s73, v188
	v_med3_f32 v27, v117, s73, v188
	v_cvt_pk_fp8_f32 v33, v25, v27 op_sel:[0,0,1]
	v_pk_fma_f32 v[30:31], v[112:113], s[16:17], v[16:17] op_sel_hi:[1,0,1]
	global_store_dwordx2 v[122:123], v[32:33], off offset:128
	v_pk_fma_f32 v[32:33], v[110:111], s[16:17], v[14:15] op_sel_hi:[1,0,1]
	v_pk_mul_f32 v[30:31], v[30:31], v[28:29] op_sel_hi:[1,0]
	v_pk_mul_f32 v[32:33], v[32:33], v[28:29] op_sel_hi:[1,0]
	v_med3_f32 v25, v30, s73, v188
	v_med3_f32 v19, v32, s73, v188
	v_med3_f32 v21, v33, s73, v188
	v_mov_b32_e32 v30, 0
	v_med3_f32 v27, v31, s73, v188
	v_cvt_pk_fp8_f32 v30, v19, v21
	v_med3_f32 v19, v106, s73, v188
	v_med3_f32 v21, v107, s73, v188
	v_mov_b32_e32 v31, 0
	v_cvt_pk_fp8_f32 v31, v19, v21
	v_cvt_pk_fp8_f32 v30, v25, v27 op_sel:[0,0,1]
	v_med3_f32 v25, v108, s73, v188
	v_med3_f32 v27, v109, s73, v188
	v_cvt_pk_fp8_f32 v31, v25, v27 op_sel:[0,0,1]
	v_add_co_u32_e32 v106, vcc, s69, v22
	v_med3_f32 v19, v102, s73, v188
	s_nop 0
	v_addc_co_u32_e32 v107, vcc, 0, v23, vcc
	global_store_dwordx2 v[106:107], v[30:31], off
	v_pk_fma_f32 v[30:31], v[104:105], s[16:17], v[8:9] op_sel_hi:[1,0,1]
	v_med3_f32 v21, v103, s73, v188
	v_pk_mul_f32 v[30:31], v[30:31], v[28:29] op_sel_hi:[1,0]
	v_pk_mul_f32 v[28:29], v[98:99], v[28:29] op_sel_hi:[1,0]
	v_med3_f32 v25, v30, s73, v188
	v_mov_b32_e32 v30, 0
	v_med3_f32 v27, v31, s73, v188
	v_cvt_pk_fp8_f32 v30, v19, v21
	v_med3_f32 v19, v28, s73, v188
	v_med3_f32 v21, v29, s73, v188
	v_mov_b32_e32 v31, 0
	v_cvt_pk_fp8_f32 v31, v19, v21
	v_cvt_pk_fp8_f32 v30, v25, v27 op_sel:[0,0,1]
	v_med3_f32 v25, v100, s73, v188
	v_med3_f32 v27, v101, s73, v188
	v_cvt_pk_fp8_f32 v31, v25, v27 op_sel:[0,0,1]
	v_lshl_add_u64 v[32:33], v[22:23], 0, s[22:23]
	v_pk_fma_f32 v[28:29], v[96:97], s[16:17], v[16:17] op_sel_hi:[1,0,1]
	v_pk_mul_f32 v[90:91], v[90:91], v[26:27] op_sel_hi:[1,0]
	global_store_dwordx2 v[32:33], v[30:31], off offset:128
	v_pk_fma_f32 v[30:31], v[94:95], s[16:17], v[14:15] op_sel_hi:[1,0,1]
	v_pk_mul_f32 v[28:29], v[28:29], v[26:27] op_sel_hi:[1,0]
	v_pk_mul_f32 v[30:31], v[30:31], v[26:27] op_sel_hi:[1,0]
	v_pk_fma_f32 v[32:33], v[92:93], s[16:17], v[12:13] op_sel_hi:[1,0,1]
	v_med3_f32 v19, v30, s73, v188
	v_med3_f32 v21, v31, s73, v188
	v_med3_f32 v25, v28, s73, v188
	v_mov_b32_e32 v28, 0
	v_pk_mul_f32 v[32:33], v[32:33], v[26:27] op_sel_hi:[1,0]
	v_med3_f32 v27, v29, s73, v188
	v_cvt_pk_fp8_f32 v28, v19, v21
	v_med3_f32 v19, v90, s73, v188
	v_med3_f32 v21, v91, s73, v188
	v_mov_b32_e32 v29, 0
	v_cvt_pk_fp8_f32 v29, v19, v21
	v_cvt_pk_fp8_f32 v28, v25, v27 op_sel:[0,0,1]
	v_med3_f32 v25, v32, s73, v188
	v_med3_f32 v27, v33, s73, v188
	v_cvt_pk_fp8_f32 v29, v25, v27 op_sel:[0,0,1]
	v_add_co_u32_e32 v32, vcc, s74, v22
	v_pk_mul_f32 v[84:85], v[84:85], v[26:27] op_sel_hi:[1,0]
	s_nop 0
	v_addc_co_u32_e32 v33, vcc, 0, v23, vcc
	global_store_dwordx2 v[32:33], v[28:29], off
	v_pk_fma_f32 v[28:29], v[88:89], s[16:17], v[8:9] op_sel_hi:[1,0,1]
	v_pk_fma_f32 v[32:33], v[86:87], s[16:17], v[6:7] op_sel_hi:[1,0,1]
	v_pk_mul_f32 v[28:29], v[28:29], v[26:27] op_sel_hi:[1,0]
	v_pk_mul_f32 v[32:33], v[32:33], v[26:27] op_sel_hi:[1,0]
	v_med3_f32 v25, v28, s73, v188
	v_med3_f32 v19, v32, s73, v188
	v_med3_f32 v21, v33, s73, v188
	v_mov_b32_e32 v28, 0
	v_cvt_pk_fp8_f32 v28, v19, v21
	v_pk_mul_f32 v[26:27], v[82:83], v[26:27] op_sel_hi:[1,0]
	v_med3_f32 v29, v29, s73, v188
	v_med3_f32 v19, v26, s73, v188
	v_cvt_pk_fp8_f32 v28, v25, v29 op_sel:[0,0,1]
	v_med3_f32 v21, v27, s73, v188
	v_mov_b32_e32 v29, 0
	v_cvt_pk_fp8_f32 v29, v19, v21
	v_med3_f32 v25, v84, s73, v188
	v_med3_f32 v26, v85, s73, v188
	v_lshl_add_u64 v[30:31], v[22:23], 0, s[6:7]
	v_cvt_pk_fp8_f32 v29, v25, v26 op_sel:[0,0,1]
	v_pk_fma_f32 v[26:27], v[80:81], s[16:17], v[16:17] op_sel_hi:[1,0,1]
	v_pk_fma_f32 v[32:33], v[74:75], s[16:17], v[10:11] op_sel_hi:[1,0,1]
	v_pk_mul_f32 v[26:27], v[26:27], v[24:25] op_sel_hi:[1,0]
	global_store_dwordx2 v[30:31], v[28:29], off offset:128
	v_pk_fma_f32 v[28:29], v[78:79], s[16:17], v[14:15] op_sel_hi:[1,0,1]
	v_pk_fma_f32 v[30:31], v[76:77], s[16:17], v[12:13] op_sel_hi:[1,0,1]
	v_pk_mul_f32 v[28:29], v[28:29], v[24:25] op_sel_hi:[1,0]
	v_pk_mul_f32 v[30:31], v[30:31], v[24:25] op_sel_hi:[1,0]
	v_pk_mul_f32 v[32:33], v[32:33], v[24:25] op_sel_hi:[1,0]
	v_med3_f32 v19, v28, s73, v188
	v_med3_f32 v21, v29, s73, v188
	v_med3_f32 v25, v26, s73, v188
	v_mov_b32_e32 v26, 0
	v_cvt_pk_fp8_f32 v26, v19, v21
	v_med3_f32 v27, v27, s73, v188
	v_med3_f32 v19, v32, s73, v188
	v_med3_f32 v21, v33, s73, v188
	v_cvt_pk_fp8_f32 v26, v25, v27 op_sel:[0,0,1]
	v_mov_b32_e32 v27, 0
	v_cvt_pk_fp8_f32 v27, v19, v21
	v_med3_f32 v25, v30, s73, v188
	v_med3_f32 v28, v31, s73, v188
	v_add_co_u32_e32 v30, vcc, s75, v22
	v_cvt_pk_fp8_f32 v27, v25, v28 op_sel:[0,0,1]
;     __device__ __forceinline__ void operator()(const f32x4 (&acc)[2][2][4][2], const Unit& u, int wr, int wc, int fr, int fq) const {
;     ...
;             for (int m = 0; m < 4; ++m) { const size_t row = (size_t)(row0 + ai * 128 + m * 16); const float gr = grv[ai][m];
; #pragma unroll
;                 for (int bj = 0; bj < 2; ++bj) { const int col = col0 + bj * 128;
;                     const f32x4 y0 = (acc[ai][bj][m][0] * F8_DESCALE + bv[bj][0]) * gr, y1 = (acc[ai][bj][m][1] * F8_DESCALE + bv[bj][1]) * gr;
;                     v2u w8; w8.x = pk4_fp8(y0[0], y0[1], y0[2], y0[3]); w8.y = pk4_fp8(y1[0], y1[1], y1[2], y1[3]); *(v2u*)(YE + row * 2048 + col) = w8; } }
	s_nop 0
	v_addc_co_u32_e32 v31, vcc, 0, v23, vcc
	v_pk_fma_f32 v[32:33], v[68:69], s[16:17], v[4:5] op_sel_hi:[1,0,1]
	global_store_dwordx2 v[30:31], v[26:27], off
	v_pk_fma_f32 v[26:27], v[72:73], s[16:17], v[8:9] op_sel_hi:[1,0,1]
	v_pk_fma_f32 v[30:31], v[70:71], s[16:17], v[6:7] op_sel_hi:[1,0,1]
	v_pk_mul_f32 v[26:27], v[26:27], v[24:25] op_sel_hi:[1,0]
	v_pk_mul_f32 v[30:31], v[30:31], v[24:25] op_sel_hi:[1,0]
	v_pk_mul_f32 v[32:33], v[32:33], v[24:25] op_sel_hi:[1,0]
	v_med3_f32 v19, v30, s73, v188
	v_med3_f32 v21, v31, s73, v188
	v_med3_f32 v30, v26, s73, v188
	v_mov_b32_e32 v26, 0
	v_cvt_pk_fp8_f32 v26, v19, v21
	v_pk_mul_f32 v[24:25], v[66:67], v[24:25] op_sel_hi:[1,0]
	v_med3_f32 v27, v27, s73, v188
	v_med3_f32 v19, v24, s73, v188
	v_cvt_pk_fp8_f32 v26, v30, v27 op_sel:[0,0,1]
	v_med3_f32 v21, v25, s73, v188
	v_mov_b32_e32 v27, 0
	v_cvt_pk_fp8_f32 v27, v19, v21
	v_med3_f32 v24, v32, s73, v188
	v_med3_f32 v25, v33, s73, v188
	v_lshl_add_u64 v[28:29], v[22:23], 0, s[24:25]
	v_cvt_pk_fp8_f32 v27, v24, v25 op_sel:[0,0,1]
	v_pk_fma_f32 v[24:25], v[64:65], s[16:17], v[16:17] op_sel_hi:[1,0,1]
	v_pk_fma_f32 v[30:31], v[58:59], s[16:17], v[10:11] op_sel_hi:[1,0,1]
	v_pk_mul_f32 v[24:25], v[24:25], v[20:21] op_sel_hi:[1,0]
	global_store_dwordx2 v[28:29], v[26:27], off offset:128
	v_pk_fma_f32 v[26:27], v[62:63], s[16:17], v[14:15] op_sel_hi:[1,0,1]
	v_pk_fma_f32 v[28:29], v[60:61], s[16:17], v[12:13] op_sel_hi:[1,0,1]
	v_pk_mul_f32 v[26:27], v[26:27], v[20:21] op_sel_hi:[1,0]
	v_pk_mul_f32 v[28:29], v[28:29], v[20:21] op_sel_hi:[1,0]
	v_pk_mul_f32 v[30:31], v[30:31], v[20:21] op_sel_hi:[1,0]
	v_med3_f32 v19, v26, s73, v188
	v_med3_f32 v21, v27, s73, v188
	v_med3_f32 v26, v24, s73, v188
	v_mov_b32_e32 v24, 0
	v_cvt_pk_fp8_f32 v24, v19, v21
	v_med3_f32 v25, v25, s73, v188
	v_med3_f32 v19, v30, s73, v188
	v_med3_f32 v21, v31, s73, v188
	v_cvt_pk_fp8_f32 v24, v26, v25 op_sel:[0,0,1]
	v_mov_b32_e32 v25, 0
	v_cvt_pk_fp8_f32 v25, v19, v21
	v_med3_f32 v26, v28, s73, v188
	v_med3_f32 v27, v29, s73, v188
	v_add_co_u32_e32 v28, vcc, s76, v22
	v_cvt_pk_fp8_f32 v25, v26, v27 op_sel:[0,0,1]
	s_nop 0
	v_addc_co_u32_e32 v29, vcc, 0, v23, vcc
	v_pk_fma_f32 v[30:31], v[52:53], s[16:17], v[4:5] op_sel_hi:[1,0,1]
	global_store_dwordx2 v[28:29], v[24:25], off
	v_pk_fma_f32 v[24:25], v[56:57], s[16:17], v[8:9] op_sel_hi:[1,0,1]
	v_pk_fma_f32 v[28:29], v[54:55], s[16:17], v[6:7] op_sel_hi:[1,0,1]
	v_pk_mul_f32 v[24:25], v[24:25], v[20:21] op_sel_hi:[1,0]
	v_pk_mul_f32 v[28:29], v[28:29], v[20:21] op_sel_hi:[1,0]
	v_pk_fma_f32 v[32:33], v[50:51], s[16:17], v[2:3] op_sel_hi:[1,0,1]
	v_med3_f32 v19, v28, s73, v188
	v_med3_f32 v28, v29, s73, v188
	v_med3_f32 v29, v24, s73, v188
	v_mov_b32_e32 v24, 0
	v_cvt_pk_fp8_f32 v24, v19, v28
	v_pk_mul_f32 v[30:31], v[30:31], v[20:21] op_sel_hi:[1,0]
	v_pk_mul_f32 v[20:21], v[32:33], v[20:21] op_sel_hi:[1,0]
	v_med3_f32 v25, v25, s73, v188
	v_med3_f32 v19, v20, s73, v188
	v_pk_fma_f32 v[14:15], v[46:47], s[16:17], v[14:15] op_sel_hi:[1,0,1]
	v_cvt_pk_fp8_f32 v24, v29, v25 op_sel:[0,0,1]
	v_med3_f32 v20, v21, s73, v188
	v_mov_b32_e32 v25, 0
	v_pk_fma_f32 v[16:17], v[48:49], s[16:17], v[16:17] op_sel_hi:[1,0,1]
	v_pk_mul_f32 v[14:15], v[14:15], v[18:19] op_sel_hi:[1,0]
	v_pk_fma_f32 v[12:13], v[44:45], s[16:17], v[12:13] op_sel_hi:[1,0,1]
	v_pk_fma_f32 v[10:11], v[42:43], s[16:17], v[10:11] op_sel_hi:[1,0,1]
	v_cvt_pk_fp8_f32 v25, v19, v20
	v_pk_mul_f32 v[16:17], v[16:17], v[18:19] op_sel_hi:[1,0]
	v_pk_mul_f32 v[12:13], v[12:13], v[18:19] op_sel_hi:[1,0]
	v_pk_mul_f32 v[10:11], v[10:11], v[18:19] op_sel_hi:[1,0]
	v_med3_f32 v19, v14, s73, v188
	v_med3_f32 v15, v15, s73, v188
	v_mov_b32_e32 v14, 0
	v_cvt_pk_fp8_f32 v14, v19, v15
	v_med3_f32 v10, v10, s73, v188
	v_med3_f32 v11, v11, s73, v188
	v_mov_b32_e32 v15, 0
	v_cvt_pk_fp8_f32 v15, v10, v11
	v_med3_f32 v16, v16, s73, v188
	v_med3_f32 v17, v17, s73, v188
	v_med3_f32 v12, v12, s73, v188
	v_med3_f32 v13, v13, s73, v188
	v_cvt_pk_fp8_f32 v14, v16, v17 op_sel:[0,0,1]
	v_cvt_pk_fp8_f32 v15, v12, v13 op_sel:[0,0,1]
	v_add_co_u32_e32 v12, vcc, s77, v22
	v_pk_fma_f32 v[6:7], v[38:39], s[16:17], v[6:7] op_sel_hi:[1,0,1]
	s_nop 0
	v_addc_co_u32_e32 v13, vcc, 0, v23, vcc
	v_pk_mul_f32 v[6:7], v[6:7], v[18:19] op_sel_hi:[1,0]
	v_pk_fma_f32 v[2:3], v[34:35], s[16:17], v[2:3] op_sel_hi:[1,0,1]
	global_store_dwordx2 v[12:13], v[14:15], off
	v_pk_mul_f32 v[2:3], v[2:3], v[18:19] op_sel_hi:[1,0]
	v_med3_f32 v12, v6, s73, v188
	v_med3_f32 v7, v7, s73, v188
	v_mov_b32_e32 v6, 0
	v_cvt_pk_fp8_f32 v6, v12, v7
	v_med3_f32 v2, v2, s73, v188
	v_med3_f32 v3, v3, s73, v188
	v_mov_b32_e32 v7, 0
	v_cvt_pk_fp8_f32 v7, v2, v3
	v_pk_fma_f32 v[8:9], v[40:41], s[16:17], v[8:9] op_sel_hi:[1,0,1]
	v_pk_fma_f32 v[4:5], v[36:37], s[16:17], v[4:5] op_sel_hi:[1,0,1]
	v_pk_mul_f32 v[8:9], v[8:9], v[18:19] op_sel_hi:[1,0]
	v_pk_mul_f32 v[4:5], v[4:5], v[18:19] op_sel_hi:[1,0]
	v_med3_f32 v21, v30, s73, v188
	v_med3_f32 v28, v31, s73, v188
	v_med3_f32 v8, v8, s73, v188
	v_med3_f32 v9, v9, s73, v188
	v_med3_f32 v4, v4, s73, v188
	v_med3_f32 v5, v5, s73, v188
	v_cvt_pk_fp8_f32 v25, v21, v28 op_sel:[0,0,1]
	v_cvt_pk_fp8_f32 v6, v8, v9 op_sel:[0,0,1]
	v_cvt_pk_fp8_f32 v7, v4, v5 op_sel:[0,0,1]
	v_lshl_add_u64 v[26:27], v[22:23], 0, s[26:27]
	v_lshl_add_u64 v[10:11], v[22:23], 0, s[28:29]
	s_andn2_b64 vcc, exec, s[38:39]
	global_store_dwordx2 v[26:27], v[24:25], off offset:128
	global_store_dwordx2 v[10:11], v[6:7], off offset:128
	s_cbranch_vccnz .LBB0_1519
	s_andn2_b64 vcc, exec, s[8:9]
	s_cbranch_vccnz .LBB0_1518
	s_barrier
	s_branch .LBB0_1518

; __global__ void __launch_bounds__(NTHR, 2) fwd(Args args) {
	.amdhsa_kernel _Z3fwd4Args
		.amdhsa_group_segment_fixed_size 0
		.amdhsa_private_segment_fixed_size 0
		.amdhsa_kernarg_size 504
		.amdhsa_user_sgpr_count 2
		.amdhsa_user_sgpr_dispatch_ptr 0
		.amdhsa_user_sgpr_queue_ptr 0
		.amdhsa_user_sgpr_kernarg_segment_ptr 1
		.amdhsa_user_sgpr_dispatch_id 0
		.amdhsa_user_sgpr_kernarg_preload_length 0
		.amdhsa_user_sgpr_kernarg_preload_offset 0
		.amdhsa_user_sgpr_private_segment_size 0
		.amdhsa_uses_dynamic_stack 0
		.amdhsa_enable_private_segment 0
		.amdhsa_system_sgpr_workgroup_id_x 1
		.amdhsa_system_sgpr_workgroup_id_y 0
		.amdhsa_system_sgpr_workgroup_id_z 0
		.amdhsa_system_sgpr_workgroup_info 0
		.amdhsa_system_vgpr_workitem_id 0
		.amdhsa_next_free_vgpr 252
		.amdhsa_next_free_sgpr 102
		.amdhsa_accum_offset 252
		.amdhsa_reserve_vcc 1
		.amdhsa_float_round_mode_32 0
		.amdhsa_float_round_mode_16_64 0
		.amdhsa_float_denorm_mode_32 3
		.amdhsa_float_denorm_mode_16_64 3
		.amdhsa_dx10_clamp 1
		.amdhsa_ieee_mode 1
		.amdhsa_fp16_overflow 0
		.amdhsa_tg_split 0
		.amdhsa_exception_fp_ieee_invalid_op 0
		.amdhsa_exception_fp_denorm_src 0
		.amdhsa_exception_fp_ieee_div_zero 0
		.amdhsa_exception_fp_ieee_overflow 0
		.amdhsa_exception_fp_ieee_underflow 0
		.amdhsa_exception_fp_ieee_inexact 0
		.amdhsa_exception_int_div_zero 0
	.end_amdhsa_kernel

; __global__ void __launch_bounds__(NTHR, 2) fwd(Args args) {
amdhsa.kernels:
  - .agpr_count:     0
    .args:
      - .offset:         0
        .size:           248
        .value_kind:     by_value
      - .offset:         248
        .size:           4
        .value_kind:     hidden_block_count_x
      - .offset:         252
        .size:           4
        .value_kind:     hidden_block_count_y
      - .offset:         256
        .size:           4
        .value_kind:     hidden_block_count_z
      - .offset:         260
        .size:           2
        .value_kind:     hidden_group_size_x
      - .offset:         262
        .size:           2
        .value_kind:     hidden_group_size_y
      - .offset:         264
        .size:           2
        .value_kind:     hidden_group_size_z
      - .offset:         266
        .size:           2
        .value_kind:     hidden_remainder_x
      - .offset:         268
        .size:           2
        .value_kind:     hidden_remainder_y
      - .offset:         270
        .size:           2
        .value_kind:     hidden_remainder_z
      - .offset:         288
        .size:           8
        .value_kind:     hidden_global_offset_x
      - .offset:         296
        .size:           8
        .value_kind:     hidden_global_offset_y
      - .offset:         304
        .size:           8
        .value_kind:     hidden_global_offset_z
      - .offset:         312
        .size:           2
        .value_kind:     hidden_grid_dims
      - .offset:         368
        .size:           4
        .value_kind:     hidden_dynamic_lds_size
    .group_segment_fixed_size: 0
    .kernarg_segment_align: 8
    .kernarg_segment_size: 504
    .language:       OpenCL C
    .language_version:
      - 2
      - 0
    .max_flat_workgroup_size: 512
    .name:           _Z3fwd4Args
    .private_segment_fixed_size: 0
    .sgpr_count:     108
    .sgpr_spill_count: 158
    .symbol:         _Z3fwd4Args.kd
    .uniform_work_group_size: 1
    .uses_dynamic_stack: false
    .vgpr_count:     252
    .vgpr_spill_count: 0
    .wavefront_size: 64
